# hyena latent unit: wave-local FFT pass barrier dropped + x1/x2 streams touched ahead of the v loads (software prefetch into L2)
# baseline (speedup 1.0000x reference)
.LBB0_1051:
	v_add_u32_e32 v3, s3, v38
	v_ashrrev_i32_e32 v7, 6, v3
	v_lshlrev_b32_e32 v7, 5, v7
	v_add3_u32 v7, v136, v7, s5
	ds_read_b64 v[54:55], v7
	v_add_u32_e32 v7, 0x200, v3
	v_ashrrev_i32_e32 v7, 6, v7
	v_lshlrev_b32_e32 v7, 5, v7
	v_add3_u32 v7, v136, v7, s5
	s_waitcnt lgkmcnt(0)
	global_store_dwordx2 v[52:53], v[54:55], off
	ds_read_b64 v[54:55], v7 offset:4096
	v_add_u32_e32 v7, 0x400, v3
	v_ashrrev_i32_e32 v7, 6, v7
	v_lshlrev_b32_e32 v7, 5, v7
	v_add3_u32 v7, v136, v7, s5
	s_waitcnt lgkmcnt(0)
	global_store_dwordx2 v[50:51], v[54:55], off
	ds_read_b64 v[54:55], v7 offset:8192
	s_addk_i32 s3, 0x800
	v_lshl_add_u64 v[50:51], v[50:51], 0, s[88:89]
	v_lshl_add_u64 v[52:53], v[52:53], 0, s[88:89]
	s_waitcnt lgkmcnt(0)
	global_store_dwordx2 v[48:49], v[54:55], off
	v_add_u32_e32 v54, 0x600, v3
	v_ashrrev_i32_e32 v3, 6, v54
	v_lshlrev_b32_e32 v3, 5, v3
	v_add3_u32 v3, v136, v3, s5
	ds_read_b64 v[56:57], v3 offset:12288
	v_ashrrev_i32_e32 v55, 31, v54
	s_addk_i32 s5, 0x4000
	v_lshl_add_u64 v[54:55], v[54:55], 3, s[18:19]
	v_lshl_add_u64 v[48:49], v[48:49], 0, s[88:89]
	s_cmp_eq_u32 s5, 0x20000
	s_waitcnt lgkmcnt(0)
	global_store_dwordx2 v[54:55], v[56:57], off
	s_cbranch_scc0 .LBB0_1051
	s_movk_i32 s22, 0x200
	s_mov_b64 s[18:19], 0
	s_and_b64 vcc, exec, s[0:1]
	s_barrier
	s_cbranch_vccz .LBB0_1044
	s_mov_b32 s53, s63
	s_lshl_b64 s[0:1], s[52:53], 14
	v_writelane_b32 v255, s0, 58
	s_nop 1
	v_writelane_b32 v255, s1, 59
	s_lshl_b64 s[0:1], s[52:53], 16
	s_add_u32 s64, s34, s0
	s_addc_u32 s65, s35, s1
	s_add_u32 s98, s64, 0x2000000
	s_addc_u32 s99, s65, 0
	v_lshl_add_u64 v[196:197], v[4:5], 2, s[98:99]
	global_load_dwordx2 v[198:199], v[196:197], off
	v_lshl_add_u64 v[196:197], v[36:37], 2, s[98:99]
	global_load_dwordx2 v[198:199], v[196:197], off
	v_lshl_add_u64 v[196:197], v[34:35], 2, s[98:99]
	global_load_dwordx2 v[198:199], v[196:197], off
	v_lshl_add_u64 v[196:197], v[32:33], 2, s[98:99]
	global_load_dwordx2 v[198:199], v[196:197], off
	v_lshl_add_u64 v[196:197], v[30:31], 2, s[98:99]
	global_load_dwordx2 v[198:199], v[196:197], off
	v_lshl_add_u64 v[196:197], v[28:29], 2, s[98:99]
	global_load_dwordx2 v[198:199], v[196:197], off
	v_lshl_add_u64 v[196:197], v[26:27], 2, s[98:99]
	global_load_dwordx2 v[198:199], v[196:197], off
	v_lshl_add_u64 v[196:197], v[24:25], 2, s[98:99]
	global_load_dwordx2 v[198:199], v[196:197], off
	v_lshl_add_u64 v[196:197], v[22:23], 2, s[98:99]
	global_load_dwordx2 v[198:199], v[196:197], off
	v_lshl_add_u64 v[196:197], v[20:21], 2, s[98:99]
	global_load_dwordx2 v[198:199], v[196:197], off
	v_lshl_add_u64 v[196:197], v[18:19], 2, s[98:99]
	global_load_dwordx2 v[198:199], v[196:197], off
	v_lshl_add_u64 v[196:197], v[16:17], 2, s[98:99]
	global_load_dwordx2 v[198:199], v[196:197], off
	v_lshl_add_u64 v[196:197], v[14:15], 2, s[98:99]
	global_load_dwordx2 v[198:199], v[196:197], off
	v_lshl_add_u64 v[196:197], v[12:13], 2, s[98:99]
	global_load_dwordx2 v[198:199], v[196:197], off
	v_lshl_add_u64 v[196:197], v[10:11], 2, s[98:99]
	global_load_dwordx2 v[198:199], v[196:197], off
	v_lshl_add_u64 v[196:197], v[8:9], 2, s[98:99]
	global_load_dwordx2 v[198:199], v[196:197], off
	s_add_u32 s98, s64, 0x4000000
	s_addc_u32 s99, s65, 0
	v_lshl_add_u64 v[196:197], v[4:5], 2, s[98:99]
	global_load_dwordx2 v[198:199], v[196:197], off
	v_lshl_add_u64 v[196:197], v[36:37], 2, s[98:99]
	global_load_dwordx2 v[198:199], v[196:197], off
	v_lshl_add_u64 v[196:197], v[34:35], 2, s[98:99]
	global_load_dwordx2 v[198:199], v[196:197], off
	v_lshl_add_u64 v[196:197], v[32:33], 2, s[98:99]
	global_load_dwordx2 v[198:199], v[196:197], off
	v_lshl_add_u64 v[196:197], v[30:31], 2, s[98:99]
	global_load_dwordx2 v[198:199], v[196:197], off
	v_lshl_add_u64 v[196:197], v[28:29], 2, s[98:99]
	global_load_dwordx2 v[198:199], v[196:197], off
	v_lshl_add_u64 v[196:197], v[26:27], 2, s[98:99]
	global_load_dwordx2 v[198:199], v[196:197], off
	v_lshl_add_u64 v[196:197], v[24:25], 2, s[98:99]
	global_load_dwordx2 v[198:199], v[196:197], off
	v_lshl_add_u64 v[196:197], v[22:23], 2, s[98:99]
	global_load_dwordx2 v[198:199], v[196:197], off
	v_lshl_add_u64 v[196:197], v[20:21], 2, s[98:99]
	global_load_dwordx2 v[198:199], v[196:197], off
	v_lshl_add_u64 v[196:197], v[18:19], 2, s[98:99]
	global_load_dwordx2 v[198:199], v[196:197], off
	v_lshl_add_u64 v[196:197], v[16:17], 2, s[98:99]
	global_load_dwordx2 v[198:199], v[196:197], off
	v_lshl_add_u64 v[196:197], v[14:15], 2, s[98:99]
	global_load_dwordx2 v[198:199], v[196:197], off
	v_lshl_add_u64 v[196:197], v[12:13], 2, s[98:99]
	global_load_dwordx2 v[198:199], v[196:197], off
	v_lshl_add_u64 v[196:197], v[10:11], 2, s[98:99]
	global_load_dwordx2 v[198:199], v[196:197], off
	v_lshl_add_u64 v[196:197], v[8:9], 2, s[98:99]
	global_load_dwordx2 v[198:199], v[196:197], off
	v_lshl_add_u64 v[40:41], v[4:5], 2, s[64:65]
	global_load_dwordx2 v[42:43], v[40:41], off
	v_lshl_add_u64 v[40:41], v[36:37], 2, s[64:65]
	global_load_dwordx2 v[44:45], v[40:41], off
	v_lshl_add_u64 v[40:41], v[34:35], 2, s[64:65]
	global_load_dwordx2 v[46:47], v[40:41], off
	v_lshl_add_u64 v[40:41], v[32:33], 2, s[64:65]
	global_load_dwordx2 v[48:49], v[40:41], off
	v_lshl_add_u64 v[40:41], v[30:31], 2, s[64:65]
	global_load_dwordx2 v[50:51], v[40:41], off
	v_lshl_add_u64 v[40:41], v[28:29], 2, s[64:65]
	global_load_dwordx2 v[52:53], v[40:41], off
	v_lshl_add_u64 v[40:41], v[26:27], 2, s[64:65]
	global_load_dwordx2 v[54:55], v[40:41], off
	v_lshl_add_u64 v[40:41], v[24:25], 2, s[64:65]
	global_load_dwordx2 v[56:57], v[40:41], off
	v_lshl_add_u64 v[40:41], v[22:23], 2, s[64:65]
	global_load_dwordx2 v[58:59], v[40:41], off
	v_lshl_add_u64 v[40:41], v[20:21], 2, s[64:65]
	global_load_dwordx2 v[60:61], v[40:41], off
	v_lshl_add_u64 v[40:41], v[18:19], 2, s[64:65]
	global_load_dwordx2 v[62:63], v[40:41], off
	v_lshl_add_u64 v[40:41], v[16:17], 2, s[64:65]
	global_load_dwordx2 v[64:65], v[40:41], off
	v_lshl_add_u64 v[40:41], v[14:15], 2, s[64:65]
	global_load_dwordx2 v[66:67], v[40:41], off
	v_lshl_add_u64 v[40:41], v[12:13], 2, s[64:65]
	s_lshl_b64 s[0:1], s[52:53], 2
	v_readlane_b32 s3, v255, 56
	global_load_dwordx2 v[68:69], v[40:41], off
	v_lshl_add_u64 v[40:41], v[10:11], 2, s[64:65]
	s_add_u32 s0, s3, s0
	v_readlane_b32 s3, v255, 57
	global_load_dwordx2 v[70:71], v[40:41], off
	v_lshl_add_u64 v[40:41], v[8:9], 2, s[64:65]
	s_addc_u32 s1, s3, s1
	global_load_dwordx2 v[72:73], v[40:41], off
	s_nop 0
	global_load_dword v40, v99, s[0:1]
	global_load_dword v3, v99, s[0:1] offset:2048
	s_mov_b32 s0, 0
	s_mov_b32 s1, s0
	v_mov_b64_e32 v[74:75], s[0:1]
	s_waitcnt vmcnt(17)
	ds_write_b64 v80, v[42:43]
	ds_write_b64 v120, v[74:75]
	s_waitcnt vmcnt(16)
	ds_write_b64 v81, v[44:45] offset:4096
	ds_write_b64 v118, v[74:75]
	s_waitcnt vmcnt(15)
	ds_write_b64 v82, v[46:47] offset:8192
	ds_write_b64 v116, v[74:75]
	s_waitcnt vmcnt(14)
	ds_write_b64 v83, v[48:49] offset:12288
	ds_write_b64 v114, v[74:75]
	s_waitcnt vmcnt(13)
	ds_write_b64 v84, v[50:51] offset:16384
	ds_write_b64 v112, v[74:75]
	s_waitcnt vmcnt(12)
	ds_write_b64 v85, v[52:53] offset:20480
	ds_write_b64 v110, v[74:75]
	s_waitcnt vmcnt(11)
	ds_write_b64 v86, v[54:55] offset:24576
	ds_write_b64 v108, v[74:75]
	s_waitcnt vmcnt(10)
	ds_write_b64 v87, v[56:57] offset:28672
	ds_write_b64 v1, v[74:75]
	s_waitcnt vmcnt(9)
	ds_write_b64 v135, v[58:59] offset:32768
	ds_write_b64 v88, v[74:75]
	s_waitcnt vmcnt(8)
	ds_write_b64 v134, v[60:61] offset:36864
	ds_write_b64 v89, v[74:75]
	s_waitcnt vmcnt(7)
	ds_write_b64 v133, v[62:63] offset:40960
	ds_write_b64 v90, v[74:75]
	s_waitcnt vmcnt(6)
	ds_write_b64 v132, v[64:65] offset:45056
	ds_write_b64 v91, v[74:75]
	s_waitcnt vmcnt(5)
	ds_write_b64 v131, v[66:67] offset:49152
	ds_write_b64 v92, v[74:75]
	s_waitcnt vmcnt(4)
	ds_write_b64 v130, v[68:69] offset:53248
	ds_write_b64 v93, v[74:75]
	s_waitcnt vmcnt(3)
	ds_write_b64 v129, v[70:71] offset:57344
	ds_write_b64 v94, v[74:75]
	s_waitcnt vmcnt(2)
	ds_write_b64 v127, v[72:73] offset:61440
	ds_write_b64 v95, v[74:75]
	s_waitcnt lgkmcnt(0)
	s_barrier
